# speedup vs baseline: 1.0360x; 1.0360x over previous
_Z9fast_mainILb0EEvPKiS1_S1_PKfPKcS3_PfS6_PiPyS6_:
	s_load_dwordx4 s[4:7], s[0:1], 0x20
	s_load_dwordx4 s[8:11], s[0:1], 0x8
	s_load_dwordx2 s[16:17], s[0:1], 0x0
	v_and_b32_e32 v1, 63, v0
	v_lshrrev_b32_e32 v8, 6, v0
	v_lshlrev_b32_e32 v150, 4, v1
	v_lshl_or_b32 v14, s2, 3, v8
	v_lshlrev_b32_e32 v14, 10, v14
	v_or_b32_e32 v14, v14, v150
	v_add_u32_e32 v212, 0x10000, v150
	v_add_u32_e32 v213, 0x18c00, v150
	v_mov_b32_e32 v151, 0
	s_waitcnt lgkmcnt(0)
	v_lshl_add_u64 v[4:5], s[4:5], 0, v[150:151]
	v_lshlrev_b32_e32 v2, 10, v8
	v_mov_b32_e32 v3, v151
	v_lshl_add_u64 v[6:7], v[4:5], 0, v[2:3]
	v_readfirstlane_b32 s3, v2
	v_or_b32_e32 v3, 0x2000, v2
	s_mov_b32 m0, s3
	s_mov_b64 s[4:5], 0x2000
	v_readfirstlane_b32 s3, v3
	global_load_lds_dwordx4 v[6:7], off
	v_lshl_add_u64 v[10:11], v[6:7], 0, s[4:5]
	s_mov_b32 m0, s3
	v_or_b32_e32 v3, 0x6000, v2
	global_load_lds_dwordx4 v[10:11], off
	v_or_b32_e32 v10, 0x4000, v2
	v_mov_b32_e32 v11, v151
	v_readfirstlane_b32 s3, v10
	v_lshl_add_u64 v[12:13], v[4:5], 0, v[10:11]
	s_mov_b32 m0, s3
	s_mov_b64 s[4:5], 0x6000
	v_readfirstlane_b32 s3, v3
	global_load_lds_dwordx4 v[12:13], off
	v_lshl_add_u64 v[10:11], v[6:7], 0, s[4:5]
	s_mov_b32 m0, s3
	v_or_b32_e32 v3, 0xa000, v2
	global_load_lds_dwordx4 v[10:11], off
	v_or_b32_e32 v10, 0x8000, v2
	v_mov_b32_e32 v11, v151
	v_readfirstlane_b32 s3, v10
	v_lshl_add_u64 v[12:13], v[4:5], 0, v[10:11]
	s_mov_b32 m0, s3
	s_mov_b64 s[4:5], 0xa000
	v_readfirstlane_b32 s3, v3
	global_load_lds_dwordx4 v[12:13], off
	v_or_b32_e32 v26, 0x60, v8
	s_movk_i32 s18, 0x63
	v_cmp_gt_u32_e32 vcc, s18, v26
	s_and_saveexec_b64 s[12:13], vcc
	s_cbranch_execz .Ld13_skip
	v_lshlrev_b32_e32 v26, 10, v26
	v_mov_b32_e32 v27, 0
	v_readfirstlane_b32 s18, v26
	v_lshl_add_u64 v[24:25], v[4:5], 0, v[26:27]
	s_mov_b32 m0, s18
	s_nop 0
	global_load_lds_dwordx4 v[24:25], off
.Ld13_skip:
	s_or_b64 exec, exec, s[12:13]
	global_load_dwordx4 v[176:179], v14, s[16:17]
	v_lshl_add_u64 v[10:11], v[6:7], 0, s[4:5]
	s_mov_b32 m0, s3
	v_or_b32_e32 v3, 0xe000, v2
	global_load_lds_dwordx4 v[10:11], off
	v_or_b32_e32 v10, 0xc000, v2
	v_mov_b32_e32 v11, v151
	v_readfirstlane_b32 s3, v10
	v_lshl_add_u64 v[12:13], v[4:5], 0, v[10:11]
	s_mov_b32 m0, s3
	s_mov_b64 s[4:5], 0xe000
	v_readfirstlane_b32 s3, v3
	global_load_lds_dwordx4 v[12:13], off
	v_lshl_add_u64 v[10:11], v[6:7], 0, s[4:5]
	s_mov_b32 m0, s3
	v_or_b32_e32 v3, 0x12000, v2
	global_load_lds_dwordx4 v[10:11], off
	v_or_b32_e32 v10, 0x10000, v2
	v_mov_b32_e32 v11, v151
	v_readfirstlane_b32 s3, v10
	v_lshl_add_u64 v[12:13], v[4:5], 0, v[10:11]
	s_mov_b32 m0, s3
	s_mov_b64 s[4:5], 0x12000
	v_readfirstlane_b32 s3, v3
	global_load_lds_dwordx4 v[12:13], off
	v_lshl_add_u64 v[10:11], v[6:7], 0, s[4:5]
	s_mov_b32 m0, s3
	s_nop 0
	global_load_lds_dwordx4 v[10:11], off
	v_or_b32_e32 v10, 0x14000, v2
	v_mov_b32_e32 v11, v151
	v_readfirstlane_b32 s3, v10
	v_lshl_add_u64 v[12:13], v[4:5], 0, v[10:11]
	s_mov_b32 m0, s3
	s_movk_i32 s3, 0x2c0
	global_load_lds_dwordx4 v[12:13], off
	v_cmp_gt_u32_e32 vcc, s3, v0
	s_and_saveexec_b64 s[4:5], vcc
	s_cbranch_execz .LBB1_2
	v_or_b32_e32 v3, 0x16000, v2
	s_mov_b64 s[12:13], 0x16000
	v_readfirstlane_b32 s3, v3
	v_lshl_add_u64 v[6:7], v[6:7], 0, s[12:13]
	s_mov_b32 m0, s3
	s_nop 0
	global_load_lds_dwordx4 v[6:7], off
.LBB1_2:
	s_or_b64 exec, exec, s[4:5]
	v_lshl_or_b32 v8, s2, 3, v8
	v_mov_b32_e32 v151, 0
	v_readfirstlane_b32 s4, v8
	s_ashr_i32 s5, s4, 31
	s_lshl_b64 s[4:5], s[4:5], 2
	s_add_u32 s8, s8, s4
	v_add_u32_e32 v172, 0x22c00, v2
	s_addc_u32 s9, s9, s5
	v_lshl_add_u32 v173, v1, 2, v172
	s_add_u32 s4, s10, s4
	ds_write_b32 v173, v151
	s_addc_u32 s5, s11, s5
	s_load_dword s12, s[6:7], 0x4000
	s_load_dword s8, s[8:9], 0x0
	v_lshrrev_b32_e32 v18, 5, v1
	s_load_dword s3, s[4:5], 0x0
	s_waitcnt lgkmcnt(0)
	s_movk_i32 s4, 0xff
	v_cmp_lt_u32_e32 vcc, s4, v0
	v_bfe_u32 v64, v0, 6, 1
	v_lshlrev_b32_e32 v174, 4, v18
	v_lshl_or_b32 v2, s8, 6, v1
	v_ashrrev_i32_e32 v3, 31, v2
	v_lshl_add_u64 v[2:3], v[2:3], 2, s[6:7]
	s_waitcnt vmcnt(8)
	s_waitcnt lgkmcnt(0)
	s_barrier
	global_load_dword v175, v[2:3], off
	s_and_saveexec_b64 s[4:5], vcc
	s_xor_b64 s[4:5], exec, s[4:5]
	s_cbranch_execz .LBB1_6
	v_lshlrev_b32_e32 v2, 2, v0
	v_and_b32_e32 v2, 0x7c, v2
	v_bfe_u32 v19, v0, 7, 1
	v_lshl_or_b32 v2, v64, 7, v2
	v_lshl_or_b32 v32, v19, 12, v150
	ds_read_b32 v2, v2 offset:35584
	ds_read_b128 v[20:23], v32
	v_lshlrev_b32_e32 v40, 12, v64
	v_or_b32_e32 v41, v40, v150
	ds_read_b128 v[24:27], v41 offset:24576
	ds_read_b128 v[28:31], v32 offset:3072
	s_waitcnt lgkmcnt(3)
	v_mov_b32_e32 v3, v2
	v_mov_b32_e32 v4, v2
	v_mov_b32_e32 v5, v2
	v_mov_b32_e32 v6, v2
	v_mov_b32_e32 v7, v2
	v_mov_b32_e32 v8, v2
	v_mov_b32_e32 v9, v2
	v_mov_b32_e32 v10, v2
	v_mov_b32_e32 v11, v2
	v_mov_b32_e32 v12, v2
	v_mov_b32_e32 v13, v2
	v_mov_b32_e32 v14, v2
	v_mov_b32_e32 v15, v2
	v_mov_b32_e32 v16, v2
	v_mov_b32_e32 v17, v2
	v_lshlrev_b32_e32 v19, 11, v19
	v_or3_b32 v19, v19, v40, v150
	s_waitcnt lgkmcnt(1)
	v_mfma_f32_32x32x16_bf16 v[2:17], v[20:23], v[24:27], v[2:17]
	ds_read_b128 v[20:23], v32 offset:1024
	ds_read_b128 v[24:27], v41 offset:25600
	ds_read_b128 v[32:35], v32 offset:2048
	ds_read_b128 v[36:39], v41 offset:26624
	v_add_u32_e32 v19, 0x20c00, v19
	s_waitcnt lgkmcnt(2)
	v_mfma_f32_32x32x16_bf16 v[2:17], v[20:23], v[24:27], v[2:17]
	ds_read_b128 v[20:23], v41 offset:27648
	s_waitcnt lgkmcnt(1)
	v_mfma_f32_32x32x16_bf16 v[2:17], v[32:35], v[36:39], v[2:17]
	s_waitcnt lgkmcnt(0)
	v_mfma_f32_32x32x16_bf16 v[2:17], v[28:31], v[20:23], v[2:17]
	s_nop 11
	v_cvt_pk_bf16_f32 v9, v8, v9
	v_cvt_pk_bf16_f32 v8, v6, v7
	v_cvt_pk_bf16_f32 v7, v4, v5
	v_cvt_pk_bf16_f32 v6, v2, v3
	v_cvt_pk_bf16_f32 v5, v16, v17
	v_cvt_pk_bf16_f32 v4, v14, v15
	v_cvt_pk_bf16_f32 v3, v12, v13
	v_cvt_pk_bf16_f32 v2, v10, v11
	ds_write_b128 v19, v[6:9]
	ds_write_b128 v19, v[2:5] offset:1024
	v_lshlrev_b32_e32 v2, 4, v18

.LBB1_8:
	s_or_b64 exec, exec, s[4:5]
	s_waitcnt vmcnt(1)
	v_mov_b32_e32 v184, 1
	v_lshl_add_u32 v180, v176, 2, v172
	v_lshl_add_u32 v181, v177, 2, v172
	v_lshl_add_u32 v182, v178, 2, v172
	v_lshl_add_u32 v183, v179, 2, v172
	s_waitcnt lgkmcnt(0)
	ds_add_u32 v180, v184
	ds_add_u32 v181, v184
	ds_add_u32 v182, v184
	ds_add_u32 v183, v184
	s_waitcnt lgkmcnt(0)
	ds_read_b32 v151, v173
	s_waitcnt lgkmcnt(0)
	v_cvt_f32_i32_e32 v185, v151
	ds_write_b32 v173, v185 offset:256
	v_add_u32_e32 v10, v172, v2
	s_waitcnt vmcnt(1) lgkmcnt(0)
	s_barrier
	ds_read_b128 v[18:21], v10 offset:256
	ds_read_b128 v[22:25], v10 offset:288
	ds_read_b128 v[82:85], v10 offset:320
	ds_read_b128 v[86:89], v10 offset:352
	ds_read_b128 v[74:77], v10 offset:384
	ds_read_b128 v[78:81], v10 offset:416
	ds_read_b128 v[2:5], v213 offset:32768
	ds_read_b128 v[6:9], v213 offset:0
	ds_read_b128 v[66:69], v10 offset:448
	ds_read_b128 v[70:73], v10 offset:480
	ds_read_b128 v[10:13], v213 offset:1024
	s_waitcnt lgkmcnt(3)
	v_pk_mul_f32 v[26:27], v[8:9], v[20:21]
	v_pk_mul_f32 v[28:29], v[6:7], v[18:19]
	ds_read_b128 v[14:17], v213 offset:8192
	s_waitcnt lgkmcnt(1)
	v_pk_mul_f32 v[12:13], v[12:13], v[24:25]
	v_pk_mul_f32 v[10:11], v[10:11], v[22:23]
	v_pk_fma_f32 v[30:31], v[8:9], v[20:21], v[12:13]
	v_pk_fma_f32 v[32:33], v[6:7], v[18:19], v[10:11]
	v_cvt_pk_bf16_f32 v9, v12, v13
	v_cvt_pk_bf16_f32 v7, v26, v27
	v_cvt_pk_bf16_f32 v8, v10, v11
	v_cvt_pk_bf16_f32 v6, v28, v29
	ds_read_b128 v[10:13], v213 offset:33792
	s_nop 0
	v_mfma_f32_32x32x16_bf16 v[34:49], v[2:5], v[6:9], 0
	ds_read_b128 v[6:9], v213 offset:9216
	s_waitcnt lgkmcnt(2)
	v_mul_f32_e32 v26, v16, v20
	v_mul_f32_e32 v27, v17, v21
	v_pk_mul_f32 v[50:51], v[14:15], v[18:19]
	s_mov_b32 s4, 0x3727c5ac
	s_waitcnt lgkmcnt(0)
	v_pk_mul_f32 v[8:9], v[8:9], v[24:25]
	v_pk_mul_f32 v[28:29], v[6:7], v[22:23]
	v_pk_fma_f32 v[90:91], v[16:17], v[20:21], v[8:9]
	v_pk_fma_f32 v[92:93], v[14:15], v[18:19], v[28:29]
	ds_read_b128 v[14:17], v213 offset:2048
	v_cvt_pk_bf16_f32 v9, v8, v9
	v_cvt_pk_bf16_f32 v7, v26, v27
	v_cvt_pk_bf16_f32 v8, v28, v29
	ds_read_b128 v[26:29], v213 offset:3072
	v_cvt_pk_bf16_f32 v6, v50, v51
	s_waitcnt lgkmcnt(1)
	v_pk_mul_f32 v[94:95], v[14:15], v[82:83]
	s_mov_b32 s0, 0x3c800000
	v_mfma_f32_32x32x16_bf16 v[50:65], v[2:5], v[6:9], 0
	v_mul_f32_e32 v2, v16, v84
	v_mul_f32_e32 v3, v17, v85
	s_waitcnt lgkmcnt(0)
	v_mul_f32_e32 v4, v28, v88
	v_mul_f32_e32 v5, v29, v89
	v_pk_mul_f32 v[6:7], v[26:27], v[86:87]
	v_pk_fma_f32 v[8:9], v[16:17], v[84:85], v[4:5]
	v_cvt_pk_bf16_f32 v3, v2, v3
	v_pk_fma_f32 v[14:15], v[14:15], v[82:83], v[6:7]
	v_pk_add_f32 v[26:27], v[8:9], v[30:31]
	v_cvt_pk_bf16_f32 v5, v4, v5
	v_cvt_pk_bf16_f32 v4, v6, v7
	ds_read_b128 v[6:9], v213 offset:10240
	v_pk_add_f32 v[28:29], v[14:15], v[32:33]
	ds_read_b128 v[14:17], v213 offset:11264
	v_cvt_pk_bf16_f32 v2, v94, v95
	s_waitcnt lgkmcnt(1)
	v_pk_mul_f32 v[30:31], v[6:7], v[82:83]
	v_mov_b64_e32 v[152:153], s[4:5]
	v_mfma_f32_32x32x16_bf16 v[34:49], v[10:13], v[2:5], v[34:49]
	v_mul_f32_e32 v2, v8, v84
	v_mul_f32_e32 v3, v9, v85
	s_waitcnt lgkmcnt(0)
	v_mul_f32_e32 v4, v16, v88
	v_mul_f32_e32 v5, v17, v89
	v_pk_mul_f32 v[14:15], v[14:15], v[86:87]
	v_pk_fma_f32 v[8:9], v[8:9], v[84:85], v[4:5]
	v_pk_fma_f32 v[6:7], v[6:7], v[82:83], v[14:15]
	v_cvt_pk_bf16_f32 v5, v4, v5
	v_cvt_pk_bf16_f32 v3, v2, v3
	v_cvt_pk_bf16_f32 v4, v14, v15
	v_pk_add_f32 v[32:33], v[8:9], v[90:91]
	v_pk_add_f32 v[90:91], v[6:7], v[92:93]
	ds_read_b128 v[6:9], v213 offset:34816
	ds_read_b128 v[14:17], v213 offset:4096
	v_cvt_pk_bf16_f32 v2, v30, v31
	s_mov_b32 s13, 0
	s_mov_b64 s[6:7], 0
	v_mfma_f32_32x32x16_bf16 v[50:65], v[10:13], v[2:5], v[50:65]
	ds_read_b128 v[2:5], v213 offset:5120
	ds_read_b128 v[10:13], v213 offset:12288
	s_waitcnt lgkmcnt(2)
	v_pk_mul_f32 v[30:31], v[16:17], v[76:77]
	v_pk_mul_f32 v[92:93], v[14:15], v[74:75]
	s_waitcnt lgkmcnt(1)
	v_pk_mul_f32 v[4:5], v[4:5], v[80:81]
	v_pk_mul_f32 v[94:95], v[2:3], v[78:79]
	v_pk_fma_f32 v[2:3], v[16:17], v[76:77], v[4:5]
	v_cvt_pk_bf16_f32 v5, v4, v5
	v_pk_add_f32 v[96:97], v[2:3], v[26:27]
	v_cvt_pk_bf16_f32 v3, v30, v31
	v_cvt_pk_bf16_f32 v4, v94, v95
	v_cvt_pk_bf16_f32 v2, v92, v93
	v_pk_fma_f32 v[14:15], v[14:15], v[74:75], v[94:95]
	s_waitcnt lgkmcnt(0)
	v_pk_mul_f32 v[30:31], v[10:11], v[74:75]
	v_mfma_f32_32x32x16_bf16 v[34:49], v[6:9], v[2:5], v[34:49]
	ds_read_b128 v[2:5], v213 offset:13312
	v_add_f32_e32 v98, v14, v28
	v_add_f32_e32 v99, v15, v29
	ds_read_b128 v[14:17], v213 offset:35840
	v_pk_mul_f32 v[26:27], v[12:13], v[76:77]
	s_waitcnt lgkmcnt(1)
	v_pk_mul_f32 v[4:5], v[4:5], v[80:81]
	v_pk_mul_f32 v[28:29], v[2:3], v[78:79]
	v_pk_fma_f32 v[2:3], v[12:13], v[76:77], v[4:5]
	v_pk_fma_f32 v[10:11], v[10:11], v[74:75], v[28:29]
	v_pk_add_f32 v[32:33], v[2:3], v[32:33]
	v_pk_add_f32 v[92:93], v[10:11], v[90:91]
	ds_read_b128 v[10:13], v213 offset:6144
	v_cvt_pk_bf16_f32 v5, v4, v5
	v_cvt_pk_bf16_f32 v3, v26, v27
	v_cvt_pk_bf16_f32 v4, v28, v29
	ds_read_b128 v[26:29], v213 offset:7168
	v_cvt_pk_bf16_f32 v2, v30, v31
	s_waitcnt lgkmcnt(1)
	v_pk_mul_f32 v[30:31], v[10:11], v[66:67]
	v_mfma_f32_32x32x16_bf16 v[50:65], v[6:9], v[2:5], v[50:65]
	v_mul_f32_e32 v2, v12, v68
	v_mul_f32_e32 v3, v13, v69
	s_waitcnt lgkmcnt(0)
	v_mul_f32_e32 v4, v28, v72
	v_mul_f32_e32 v5, v29, v73
	v_pk_mul_f32 v[6:7], v[26:27], v[70:71]
	v_pk_fma_f32 v[8:9], v[12:13], v[68:69], v[4:5]
	v_cvt_pk_bf16_f32 v3, v2, v3
	v_pk_fma_f32 v[10:11], v[10:11], v[66:67], v[6:7]
	v_pk_add_f32 v[94:95], v[8:9], v[96:97]
	v_cvt_pk_bf16_f32 v5, v4, v5
	v_cvt_pk_bf16_f32 v4, v6, v7
	ds_read_b128 v[6:9], v213 offset:14336
	v_pk_add_f32 v[96:97], v[10:11], v[98:99]
	ds_read_b128 v[10:13], v213 offset:15360
	v_cvt_pk_bf16_f32 v2, v30, v31
	s_waitcnt lgkmcnt(1)
	v_pk_mul_f32 v[30:31], v[6:7], v[66:67]
	v_mfma_f32_32x32x16_bf16 v[34:49], v[14:17], v[2:5], v[34:49]
	s_waitcnt lgkmcnt(0)
	v_mul_f32_e32 v10, v10, v70
	v_mul_f32_e32 v11, v11, v71
	v_mul_f32_e32 v2, v8, v68
	v_mul_f32_e32 v3, v9, v69
	v_pk_mul_f32 v[4:5], v[12:13], v[72:73]
	v_pk_fma_f32 v[6:7], v[6:7], v[66:67], v[10:11]
	v_pk_fma_f32 v[8:9], v[8:9], v[68:69], v[4:5]
	v_pk_add_f32 v[92:93], v[6:7], v[92:93]
	v_cvt_pk_bf16_f32 v3, v2, v3
	v_pk_add_f32 v[90:91], v[8:9], v[32:33]
	v_cvt_pk_bf16_f32 v5, v4, v5
	v_cvt_pk_bf16_f32 v4, v10, v11
	ds_read_b128 v[26:29], v213 offset:36864
	ds_read_b128 v[6:9], v213 offset:16384
	v_cvt_pk_bf16_f32 v2, v30, v31
	ds_read_b128 v[98:101], v213 offset:25600
	ds_read_b128 v[102:105], v213 offset:37888
	v_mfma_f32_32x32x16_bf16 v[50:65], v[14:17], v[2:5], v[50:65]
	ds_read_b128 v[2:5], v213 offset:17408
	ds_read_b128 v[30:33], v213 offset:24576
	s_waitcnt lgkmcnt(4)
	v_pk_mul_f32 v[12:13], v[6:7], v[18:19]
	v_pk_mul_f32 v[10:11], v[8:9], v[20:21]
	s_waitcnt lgkmcnt(1)
	v_pk_mul_f32 v[14:15], v[2:3], v[22:23]
	v_pk_mul_f32 v[22:23], v[98:99], v[22:23]
	v_pk_fma_f32 v[112:113], v[6:7], v[18:19], v[14:15]
	s_waitcnt lgkmcnt(0)
	v_pk_mul_f32 v[114:115], v[30:31], v[18:19]
	v_pk_fma_f32 v[118:119], v[30:31], v[18:19], v[22:23]
	v_pk_mul_f32 v[4:5], v[4:5], v[24:25]
	v_pk_mul_f32 v[106:107], v[32:33], v[20:21]
	v_pk_mul_f32 v[24:25], v[100:101], v[24:25]
	ds_read_b128 v[98:101], v213 offset:18432
	v_cvt_pk_bf16_f32 v19, v106, v107
	ds_read_b128 v[106:109], v213 offset:19456
	v_pk_fma_f32 v[110:111], v[8:9], v[20:21], v[4:5]
	v_cvt_pk_bf16_f32 v5, v4, v5
	v_cvt_pk_bf16_f32 v3, v10, v11
	v_cvt_pk_bf16_f32 v4, v14, v15
	s_waitcnt lgkmcnt(0)
	v_pk_mul_f32 v[106:107], v[106:107], v[86:87]
	v_cvt_pk_bf16_f32 v2, v12, v13
	v_pk_mul_f32 v[120:121], v[98:99], v[82:83]
	v_pk_mul_f32 v[108:109], v[108:109], v[88:89]
	v_pk_fma_f32 v[98:99], v[98:99], v[82:83], v[106:107]
	v_mfma_f32_32x32x16_bf16 v[2:17], v[26:29], v[2:5], 0
	v_cvt_pk_bf16_f32 v18, v114, v115
	v_mul_f32_e32 v114, v100, v84
	v_mul_f32_e32 v115, v101, v85
	v_fma_f32 v100, v100, v84, v108
	v_fma_f32 v101, v101, v85, v109
	v_pk_add_f32 v[124:125], v[98:99], v[112:113]
	v_pk_add_f32 v[122:123], v[100:101], v[110:111]
	v_cvt_pk_bf16_f32 v101, v108, v109
	v_cvt_pk_bf16_f32 v100, v106, v107
	ds_read_b128 v[106:109], v213 offset:26624
	v_pk_fma_f32 v[116:117], v[32:33], v[20:21], v[24:25]
	v_cvt_pk_bf16_f32 v21, v24, v25
	v_cvt_pk_bf16_f32 v20, v22, v23
	ds_read_b128 v[110:113], v213 offset:27648
	v_cvt_pk_bf16_f32 v99, v114, v115
	v_mfma_f32_32x32x16_bf16 v[18:33], v[26:29], v[18:21], 0
	v_cvt_pk_bf16_f32 v98, v120, v121
	s_waitcnt lgkmcnt(1)
	v_mul_f32_e32 v114, v106, v82
	v_mul_f32_e32 v115, v107, v83
	s_waitcnt lgkmcnt(0)
	v_pk_mul_f32 v[86:87], v[110:111], v[86:87]
	v_pk_mul_f32 v[88:89], v[112:113], v[88:89]
	v_pk_fma_f32 v[82:83], v[106:107], v[82:83], v[86:87]
	v_mfma_f32_32x32x16_bf16 v[2:17], v[102:105], v[98:101], v[2:17]
	v_mul_f32_e32 v98, v108, v84
	v_mul_f32_e32 v99, v109, v85
	v_fma_f32 v84, v108, v84, v88
	v_fma_f32 v85, v109, v85, v89
	v_add_f32_e32 v108, v82, v118
	v_add_f32_e32 v109, v83, v119
	v_cvt_pk_bf16_f32 v83, v98, v99
	v_pk_add_f32 v[106:107], v[84:85], v[116:117]
	v_cvt_pk_bf16_f32 v85, v88, v89
	v_cvt_pk_bf16_f32 v84, v86, v87
	ds_read_b128 v[86:89], v213 offset:38912
	ds_read_b128 v[98:101], v213 offset:20480
	v_cvt_pk_bf16_f32 v82, v114, v115
	s_waitcnt lgkmcnt(0)
	v_pk_mul_f32 v[110:111], v[100:101], v[76:77]
	v_mfma_f32_32x32x16_bf16 v[18:33], v[102:105], v[82:85], v[18:33]
	ds_read_b128 v[82:85], v213 offset:21504
	ds_read_b128 v[102:105], v213 offset:28672
	v_mul_f32_e32 v112, v98, v74
	v_mul_f32_e32 v113, v99, v75
	s_waitcnt lgkmcnt(1)
	v_pk_mul_f32 v[84:85], v[84:85], v[80:81]
	v_pk_mul_f32 v[114:115], v[82:83], v[78:79]
	v_pk_fma_f32 v[82:83], v[100:101], v[76:77], v[84:85]
	v_cvt_pk_bf16_f32 v85, v84, v85
	v_pk_add_f32 v[116:117], v[82:83], v[122:123]
	v_cvt_pk_bf16_f32 v83, v110, v111
	v_cvt_pk_bf16_f32 v84, v114, v115
	v_cvt_pk_bf16_f32 v82, v112, v113
	v_pk_fma_f32 v[98:99], v[98:99], v[74:75], v[114:115]
	s_waitcnt lgkmcnt(0)
	v_pk_mul_f32 v[112:113], v[102:103], v[74:75]
	v_mfma_f32_32x32x16_bf16 v[2:17], v[86:89], v[82:85], v[2:17]
	ds_read_b128 v[82:85], v213 offset:29696
	v_add_f32_e32 v118, v98, v124
	v_add_f32_e32 v119, v99, v125
	v_mul_f32_e32 v110, v104, v76
	v_mul_f32_e32 v111, v105, v77
	ds_read_b128 v[98:101], v213 offset:39936
	s_waitcnt lgkmcnt(1)
	v_pk_mul_f32 v[78:79], v[82:83], v[78:79]
	v_pk_mul_f32 v[80:81], v[84:85], v[80:81]
	v_pk_fma_f32 v[74:75], v[102:103], v[74:75], v[78:79]
	v_pk_fma_f32 v[76:77], v[104:105], v[76:77], v[80:81]
	v_pk_add_f32 v[104:105], v[74:75], v[108:109]
	v_pk_add_f32 v[102:103], v[76:77], v[106:107]
	v_cvt_pk_bf16_f32 v77, v80, v81
	v_cvt_pk_bf16_f32 v76, v78, v79
	ds_read_b128 v[78:81], v213 offset:22528
	ds_read_b128 v[82:85], v213 offset:23552
	v_cvt_pk_bf16_f32 v75, v110, v111
	v_cvt_pk_bf16_f32 v74, v112, v113
	s_waitcnt lgkmcnt(0)
	v_pk_mul_f32 v[82:83], v[82:83], v[70:71]
	v_mfma_f32_32x32x16_bf16 v[18:33], v[86:89], v[74:77], v[18:33]
	v_mul_f32_e32 v74, v80, v68
	v_mul_f32_e32 v75, v81, v69
	v_mul_f32_e32 v76, v84, v72
	v_mul_f32_e32 v77, v85, v73
	v_mul_f32_e32 v86, v78, v66
	v_mul_f32_e32 v87, v79, v67
	v_pk_fma_f32 v[80:81], v[80:81], v[68:69], v[76:77]
	v_pk_fma_f32 v[78:79], v[78:79], v[66:67], v[82:83]
	v_cvt_pk_bf16_f32 v75, v74, v75
	v_pk_add_f32 v[88:89], v[80:81], v[116:117]
	v_pk_add_f32 v[106:107], v[78:79], v[118:119]
	ds_read_b128 v[78:81], v213 offset:30720
	v_cvt_pk_bf16_f32 v77, v76, v77
	v_cvt_pk_bf16_f32 v76, v82, v83
	ds_read_b128 v[82:85], v213 offset:31744
	v_cvt_pk_bf16_f32 v74, v86, v87
	s_waitcnt lgkmcnt(0)
	v_pk_mul_f32 v[72:73], v[84:85], v[72:73]
	v_mfma_f32_32x32x16_bf16 v[2:17], v[98:101], v[74:77], v[2:17]
	v_mul_f32_e32 v74, v80, v68
	v_mul_f32_e32 v75, v81, v69
	v_fma_f32 v68, v80, v68, v72
	v_fma_f32 v69, v81, v69, v73
	v_mul_f32_e32 v70, v82, v70
	v_mul_f32_e32 v71, v83, v71
	v_pk_add_f32 v[84:85], v[68:69], v[102:103]
	v_cvt_pk_bf16_f32 v69, v72, v73
	v_pk_mov_b32 v[72:73], v[96:97], v[94:95] op_sel:[1,0]
	v_mov_b32_e32 v97, v95
	v_pk_add_f32 v[72:73], v[72:73], v[96:97]
	v_pk_mul_f32 v[76:77], v[78:79], v[66:67]
	v_pk_fma_f32 v[66:67], v[78:79], v[66:67], v[70:71]
	v_pk_add_f32 v[72:73], v[72:73], v[72:73] op_sel:[0,1] op_sel_hi:[1,0]
	v_pk_add_f32 v[86:87], v[66:67], v[104:105]
	v_mov_b32_e32 v66, v72
	s_nop 1
	v_permlane32_swap_b32_e32 v72, v66
	v_add_f32_e32 v66, v72, v66
	v_cvt_pk_bf16_f32 v67, v74, v75
	v_rcp_f32_e32 v74, v66
	v_cvt_pk_bf16_f32 v68, v70, v71
	v_cvt_pk_bf16_f32 v66, v76, v77
	v_pk_mul_f32 v[70:71], v[46:47], v[74:75] op_sel_hi:[1,0]
	s_nop 0
	v_mfma_f32_32x32x16_bf16 v[18:33], v[98:101], v[66:69], v[18:33]
	v_mul_f32_e32 v66, v42, v74
	v_mul_f32_e32 v67, v43, v74
	v_pk_mov_b32 v[42:43], v[92:93], v[90:91] op_sel:[1,0]
	v_mov_b32_e32 v93, v91
	v_pk_add_f32 v[42:43], v[42:43], v[92:93]
	v_pk_mul_f32 v[68:69], v[44:45], v[74:75] op_sel_hi:[1,0]
	v_pk_add_f32 v[42:43], v[42:43], v[42:43] op_sel:[0,1] op_sel_hi:[1,0]
	v_pk_mov_b32 v[44:45], v[106:107], v[88:89] op_sel:[1,0]
	v_mov_b32_e32 v43, v42
	s_nop 1
	v_permlane32_swap_b32_e32 v42, v43
	v_add_f32_e32 v42, v42, v43
	v_rcp_f32_e32 v42, v42
	v_mov_b32_e32 v107, v89
	v_pk_add_f32 v[44:45], v[44:45], v[106:107]
	v_pk_mul_f32 v[72:73], v[48:49], v[74:75] op_sel_hi:[1,0]
	v_pk_add_f32 v[44:45], v[44:45], v[44:45] op_sel:[0,1] op_sel_hi:[1,0]
	v_pk_mul_f32 v[36:37], v[36:37], v[74:75] op_sel_hi:[1,0]
	v_pk_mul_f32 v[38:39], v[38:39], v[74:75] op_sel_hi:[1,0]
	v_pk_mul_f32 v[40:41], v[40:41], v[74:75] op_sel_hi:[1,0]
	v_pk_mul_f32 v[34:35], v[34:35], v[74:75] op_sel_hi:[1,0]
	v_pk_mul_f32 v[74:75], v[58:59], v[42:43] op_sel_hi:[1,0]
	v_pk_mul_f32 v[78:79], v[60:61], v[42:43] op_sel_hi:[1,0]
	v_pk_mul_f32 v[80:81], v[62:63], v[42:43] op_sel_hi:[1,0]
	v_pk_mul_f32 v[82:83], v[64:65], v[42:43] op_sel_hi:[1,0]
	v_pk_mul_f32 v[92:93], v[52:53], v[42:43] op_sel_hi:[1,0]
	v_mov_b32_e32 v43, v44
	s_nop 1
	v_permlane32_swap_b32_e32 v44, v43
	v_add_f32_e32 v43, v44, v43
	v_rcp_f32_e32 v76, v43
	v_pk_mul_f32 v[96:97], v[54:55], v[42:43] op_sel_hi:[1,0]
	v_pk_mul_f32 v[94:95], v[56:57], v[42:43] op_sel_hi:[1,0]
	v_pk_mul_f32 v[98:99], v[50:51], v[42:43] op_sel_hi:[1,0]
	v_pk_mul_f32 v[100:101], v[4:5], v[76:77] op_sel_hi:[1,0]
	v_pk_mov_b32 v[4:5], v[86:87], v[84:85] op_sel:[1,0]
	v_mov_b32_e32 v87, v85
	v_pk_add_f32 v[4:5], v[4:5], v[86:87]
	v_pk_mul_f32 v[102:103], v[6:7], v[76:77] op_sel_hi:[1,0]
	v_pk_add_f32 v[104:105], v[4:5], v[4:5] op_sel:[0,1] op_sel_hi:[1,0]
	v_cvt_pk_bf16_f32 v7, v40, v41
	ds_read_b128 v[84:87], v150 offset:52224
	ds_read_b128 v[50:53], v150 offset:35840
	ds_read_b128 v[54:57], v150 offset:36864
	ds_read_b128 v[58:61], v150 offset:37888
	ds_read_b128 v[62:65], v150 offset:38912
	v_cvt_pk_bf16_f32 v6, v38, v39
	v_cvt_pk_bf16_f32 v5, v36, v37
	v_cvt_pk_bf16_f32 v4, v34, v35
	ds_read_b128 v[88:91], v150 offset:53248
	ds_read_b128 v[34:37], v150 offset:39936
	ds_read_b128 v[38:41], v150 offset:40960
	ds_read_b128 v[42:45], v150 offset:41984
	ds_read_b128 v[46:49], v150 offset:43008
	v_cvt_pk_bf16_f32 v95, v94, v95
	v_cvt_pk_bf16_f32 v94, v96, v97
	v_cvt_pk_bf16_f32 v93, v92, v93
	v_cvt_pk_bf16_f32 v92, v98, v99
	s_waitcnt lgkmcnt(5)
	v_mfma_f32_32x32x16_bf16 v[50:65], v[84:87], v[4:7], v[50:65]
	v_mul_f32_e32 v10, v10, v76
	v_mul_f32_e32 v11, v11, v76
	v_mul_f32_e32 v12, v12, v76
	v_mul_f32_e32 v13, v13, v76
	v_mul_f32_e32 v8, v8, v76
	v_mul_f32_e32 v9, v9, v76
	v_mov_b32_e32 v77, v104
	s_nop 1
	v_permlane32_swap_b32_e32 v104, v77
	v_cvt_pk_bf16_f32 v73, v72, v73
	s_waitcnt lgkmcnt(0)
	v_mfma_f32_32x32x16_bf16 v[34:49], v[84:87], v[92:95], v[34:49]
	v_cvt_pk_bf16_f32 v72, v70, v71
	v_cvt_pk_bf16_f32 v70, v66, v67
	v_add_f32_e32 v66, v104, v77
	v_cvt_pk_bf16_f32 v71, v68, v69
	v_rcp_f32_e32 v104, v66
	v_cvt_pk_bf16_f32 v69, v82, v83
	v_cvt_pk_bf16_f32 v68, v80, v81
	v_cvt_pk_bf16_f32 v67, v78, v79
	v_cvt_pk_bf16_f32 v66, v74, v75
	ds_read_b128 v[78:81], v150 offset:54272
	v_mfma_f32_32x32x16_bf16 v[50:65], v[88:91], v[70:73], v[50:65]
	v_mul_f32_e32 v2, v2, v76
	v_mul_f32_e32 v3, v3, v76
	v_mul_f32_e32 v20, v20, v104
	v_mul_f32_e32 v21, v21, v104
	v_cvt_pk_bf16_f32 v85, v8, v9
	v_cvt_pk_bf16_f32 v82, v2, v3
	v_pk_mul_f32 v[2:3], v[22:23], v[104:105] op_sel_hi:[1,0]
	v_pk_mul_f32 v[8:9], v[24:25], v[104:105] op_sel_hi:[1,0]
	v_pk_mul_f32 v[18:19], v[18:19], v[104:105] op_sel_hi:[1,0]
	v_mfma_f32_32x32x16_bf16 v[34:49], v[88:91], v[66:69], v[34:49]
	v_cvt_pk_bf16_f32 v84, v102, v103
	v_cvt_pk_bf16_f32 v83, v100, v101
	ds_read_b128 v[86:89], v150 offset:55296
	v_cvt_pk_bf16_f32 v99, v8, v9
	v_cvt_pk_bf16_f32 v98, v2, v3
	v_cvt_pk_bf16_f32 v97, v20, v21
	v_cvt_pk_bf16_f32 v96, v18, v19
	s_waitcnt lgkmcnt(1)
	v_mfma_f32_32x32x16_bf16 v[50:65], v[78:81], v[82:85], v[50:65]
	v_mul_f32_e32 v2, v14, v76
	v_mul_f32_e32 v3, v15, v76
	v_mul_f32_e32 v8, v16, v76
	v_mul_f32_e32 v9, v17, v76
	v_mul_f32_e32 v14, v26, v104
	v_mul_f32_e32 v15, v27, v104
	v_cvt_pk_bf16_f32 v77, v8, v9
	v_cvt_pk_bf16_f32 v76, v2, v3
	v_cvt_pk_bf16_f32 v74, v10, v11
	v_pk_mul_f32 v[2:3], v[28:29], v[104:105] op_sel_hi:[1,0]
	v_mfma_f32_32x32x16_bf16 v[34:49], v[78:81], v[96:99], v[34:49]
	v_mul_f32_e32 v8, v30, v104
	v_mul_f32_e32 v9, v31, v104
	v_mul_f32_e32 v10, v32, v104
	v_mul_f32_e32 v11, v33, v104
	v_cvt_pk_bf16_f32 v75, v12, v13
	v_cvt_pk_bf16_f32 v81, v10, v11
	v_cvt_pk_bf16_f32 v80, v8, v9
	v_cvt_pk_bf16_f32 v79, v2, v3
	v_cvt_pk_bf16_f32 v78, v14, v15
	s_waitcnt lgkmcnt(0)
	v_mfma_f32_32x32x16_bf16 v[50:65], v[86:89], v[74:77], v[50:65]
	v_mfma_f32_32x32x16_bf16 v[34:49], v[86:89], v[78:81], v[34:49]
	ds_read_b128 v[86:89], v150 offset:56320
	ds_read_b128 v[18:21], v150 offset:44032
	ds_read_b128 v[22:25], v150 offset:45056
	ds_read_b128 v[26:29], v150 offset:46080
	ds_read_b128 v[30:33], v150 offset:47104
	ds_read_b128 v[100:103], v150 offset:57344
	s_waitcnt lgkmcnt(1)
	v_mfma_f32_32x32x16_bf16 v[18:33], v[86:89], v[4:7], v[18:33]
	ds_read_b128 v[2:5], v150 offset:48128
	ds_read_b128 v[6:9], v150 offset:49152
	ds_read_b128 v[10:13], v150 offset:50176
	ds_read_b128 v[14:17], v150 offset:51200
	s_waitcnt lgkmcnt(0)
	v_mfma_f32_32x32x16_bf16 v[2:17], v[86:89], v[92:95], v[2:17]
	v_mfma_f32_32x32x16_bf16 v[18:33], v[100:103], v[70:73], v[18:33]
	v_mfma_f32_32x32x16_bf16 v[2:17], v[100:103], v[66:69], v[2:17]
	ds_read_b128 v[66:69], v150 offset:58368
	ds_read_b128 v[70:73], v150 offset:59392
	s_waitcnt lgkmcnt(1)
	v_mfma_f32_32x32x16_bf16 v[18:33], v[66:69], v[82:85], v[18:33]
	v_mfma_f32_32x32x16_bf16 v[2:17], v[66:69], v[96:99], v[2:17]
	s_waitcnt lgkmcnt(0)
	v_mfma_f32_32x32x16_bf16 v[18:33], v[70:73], v[74:77], v[18:33]
	v_mfma_f32_32x32x16_bf16 v[2:17], v[70:73], v[78:81], v[2:17]
	s_nop 10
	v_mul_f32_e32 v66, v22, v22
	v_mul_f32_e32 v67, v23, v23
	v_mul_f32_e32 v68, v30, v30
	v_mul_f32_e32 v69, v31, v31
	v_mul_f32_e32 v70, v24, v24
	v_mul_f32_e32 v71, v25, v25
	v_pk_mul_f32 v[72:73], v[32:33], v[32:33]
	v_pk_mul_f32 v[74:75], v[20:21], v[20:21]
	v_pk_mul_f32 v[76:77], v[28:29], v[28:29]
	v_pk_mul_f32 v[78:79], v[26:27], v[26:27]
	v_pk_mul_f32 v[80:81], v[18:19], v[18:19]
	v_pk_fma_f32 v[78:79], v[58:59], v[58:59], v[78:79]
	v_pk_fma_f32 v[76:77], v[60:61], v[60:61], v[76:77]
	v_pk_fma_f32 v[74:75], v[52:53], v[52:53], v[74:75]
	v_pk_fma_f32 v[72:73], v[64:65], v[64:65], v[72:73]
	v_pk_fma_f32 v[70:71], v[56:57], v[56:57], v[70:71]
	v_pk_fma_f32 v[68:69], v[62:63], v[62:63], v[68:69]
	v_pk_fma_f32 v[66:67], v[54:55], v[54:55], v[66:67]
	v_pk_fma_f32 v[80:81], v[50:51], v[50:51], v[80:81]
	v_pk_add_f32 v[66:67], v[66:67], v[68:69]
	v_pk_add_f32 v[68:69], v[70:71], v[72:73]
	v_pk_add_f32 v[70:71], v[74:75], v[76:77]
	v_pk_add_f32 v[72:73], v[80:81], v[78:79]
	v_pk_add_f32 v[68:69], v[70:71], v[68:69]
	v_pk_add_f32 v[66:67], v[72:73], v[66:67]
	v_pk_mul_f32 v[72:73], v[14:15], v[14:15]
	v_pk_mov_b32 v[70:71], v[66:67], v[68:69] op_sel:[1,0]
	v_mov_b32_e32 v67, v69
	v_pk_add_f32 v[66:67], v[70:71], v[66:67]
	v_pk_mul_f32 v[70:71], v[6:7], v[6:7]
	v_pk_mul_f32 v[74:75], v[8:9], v[8:9]
	v_pk_mul_f32 v[76:77], v[16:17], v[16:17]
	v_pk_mul_f32 v[78:79], v[4:5], v[4:5]
	v_pk_mul_f32 v[80:81], v[12:13], v[12:13]
	v_pk_mul_f32 v[82:83], v[10:11], v[10:11]
	v_pk_mul_f32 v[84:85], v[2:3], v[2:3]
	v_pk_fma_f32 v[82:83], v[42:43], v[42:43], v[82:83]
	v_pk_fma_f32 v[80:81], v[44:45], v[44:45], v[80:81]
	v_pk_fma_f32 v[78:79], v[36:37], v[36:37], v[78:79]
	v_pk_fma_f32 v[76:77], v[48:49], v[48:49], v[76:77]
	v_pk_fma_f32 v[74:75], v[40:41], v[40:41], v[74:75]
	v_pk_fma_f32 v[72:73], v[46:47], v[46:47], v[72:73]
	v_pk_fma_f32 v[70:71], v[38:39], v[38:39], v[70:71]
	v_pk_fma_f32 v[84:85], v[34:35], v[34:35], v[84:85]
	v_pk_add_f32 v[70:71], v[70:71], v[72:73]
	v_pk_add_f32 v[72:73], v[74:75], v[76:77]
	v_pk_add_f32 v[74:75], v[78:79], v[80:81]
	v_pk_add_f32 v[76:77], v[84:85], v[82:83]
	v_pk_add_f32 v[72:73], v[74:75], v[72:73]
	v_pk_add_f32 v[70:71], v[76:77], v[70:71]
	v_pk_add_f32 v[66:67], v[66:67], v[66:67] op_sel:[0,1] op_sel_hi:[1,0]
	v_pk_mov_b32 v[74:75], v[70:71], v[72:73] op_sel:[1,0]
	v_mov_b32_e32 v71, v73
	v_pk_add_f32 v[70:71], v[74:75], v[70:71]
	v_mov_b32_e32 v69, v66
	v_pk_add_f32 v[70:71], v[70:71], v[70:71] op_sel:[0,1] op_sel_hi:[1,0]
	s_nop 0
	v_permlane32_swap_b32_e32 v66, v69
	v_mov_b32_e32 v68, v70
	s_nop 1
	v_permlane32_swap_b32_e32 v70, v68
	v_mov_b32_e32 v71, v66
	v_pk_add_f32 v[66:67], v[70:71], v[68:69]
	v_pk_fma_f32 v[66:67], v[66:67], s[0:1], v[152:153] op_sel_hi:[1,0,0]
	s_mov_b32 s1, 0x800000
	v_mul_f32_e32 v68, 0x4b800000, v67
	v_cmp_gt_f32_e32 vcc, s1, v67
	s_nop 1
	v_cndmask_b32_e32 v67, v67, v68, vcc
	v_rsq_f32_e32 v67, v67
	s_nop 0
	v_mul_f32_e32 v68, 0x45800000, v67
	v_cndmask_b32_e32 v68, v67, v68, vcc
	v_pk_mul_f32 v[158:159], v[50:51], v[68:69] op_sel_hi:[1,0]
	v_pk_mul_f32 v[50:51], v[18:19], v[68:69] op_sel_hi:[1,0]
	v_mul_f32_e32 v18, 0x4b800000, v66
	v_cmp_gt_f32_e32 vcc, s1, v66
	v_pk_mul_f32 v[80:81], v[60:61], v[68:69] op_sel_hi:[1,0]
	v_pk_mul_f32 v[60:61], v[28:29], v[68:69] op_sel_hi:[1,0]
	v_cndmask_b32_e32 v18, v66, v18, vcc
	v_rsq_f32_e32 v18, v18
	v_pk_mul_f32 v[78:79], v[58:59], v[68:69] op_sel_hi:[1,0]
	v_pk_mul_f32 v[160:161], v[52:53], v[68:69] op_sel_hi:[1,0]
	v_pk_mul_f32 v[82:83], v[54:55], v[68:69] op_sel_hi:[1,0]
	v_mul_f32_e32 v19, 0x45800000, v18
	v_cndmask_b32_e32 v28, v18, v19, vcc
	v_pk_mul_f32 v[168:169], v[56:57], v[68:69] op_sel_hi:[1,0]
	v_pk_mul_f32 v[58:59], v[26:27], v[68:69] op_sel_hi:[1,0]
	v_pk_mul_f32 v[52:53], v[20:21], v[68:69] op_sel_hi:[1,0]
	v_pk_mul_f32 v[54:55], v[22:23], v[68:69] op_sel_hi:[1,0]
	v_pk_mul_f32 v[56:57], v[24:25], v[68:69] op_sel_hi:[1,0]
	v_pk_mul_f32 v[18:19], v[42:43], v[28:29] op_sel_hi:[1,0]
	v_pk_mul_f32 v[20:21], v[44:45], v[28:29] op_sel_hi:[1,0]
	v_pk_mul_f32 v[22:23], v[46:47], v[28:29] op_sel_hi:[1,0]
	v_pk_mul_f32 v[26:27], v[48:49], v[28:29] op_sel_hi:[1,0]
	v_pk_mul_f32 v[162:163], v[34:35], v[28:29] op_sel_hi:[1,0]
	v_pk_mul_f32 v[164:165], v[36:37], v[28:29] op_sel_hi:[1,0]
	v_pk_mul_f32 v[166:167], v[38:39], v[28:29] op_sel_hi:[1,0]
	v_pk_mul_f32 v[24:25], v[40:41], v[28:29] op_sel_hi:[1,0]
	v_pk_mul_f32 v[104:105], v[2:3], v[28:29] op_sel_hi:[1,0]
	v_pk_mul_f32 v[112:113], v[4:5], v[28:29] op_sel_hi:[1,0]
	ds_read_b128 v[2:5], v150 offset:60416
	ds_read_b128 v[34:37], v174 offset:32768
	ds_read_b128 v[38:41], v174 offset:32800
	ds_read_b128 v[42:45], v174 offset:32832
	ds_read_b128 v[46:49], v174 offset:32864
	v_cvt_pk_bf16_f32 v129, v168, v169
	v_cvt_pk_bf16_f32 v128, v82, v83
	v_cvt_pk_bf16_f32 v127, v160, v161
	v_cvt_pk_bf16_f32 v126, v158, v159
	v_cvt_pk_bf16_f32 v137, v24, v25
	v_cvt_pk_bf16_f32 v136, v166, v167
	v_cvt_pk_bf16_f32 v135, v164, v165
	s_waitcnt lgkmcnt(0)
	v_mfma_f32_32x32x16_bf16 v[86:101], v[2:5], v[126:129], v[34:49]
	v_cvt_pk_bf16_f32 v134, v162, v163
	v_mul_f32_e32 v84, v62, v68
	v_mul_f32_e32 v85, v63, v68
	v_mul_f32_e32 v170, v64, v68
	v_mul_f32_e32 v171, v65, v68
	v_pk_mul_f32 v[62:63], v[30:31], v[68:69] op_sel_hi:[1,0]
	v_pk_mul_f32 v[64:65], v[32:33], v[68:69] op_sel_hi:[1,0]
	v_pk_mul_f32 v[116:117], v[6:7], v[28:29] op_sel_hi:[1,0]
	v_pk_mul_f32 v[154:155], v[8:9], v[28:29] op_sel_hi:[1,0]
	v_mfma_f32_32x32x16_bf16 v[34:49], v[2:5], v[134:137], v[34:49]
	ds_read_b128 v[6:9], v150 offset:61440
	ds_read_b128 v[66:69], v174 offset:32896
	ds_read_b128 v[106:109], v150 offset:64512
	v_cvt_pk_bf16_f32 v125, v170, v171
	v_cvt_pk_bf16_f32 v124, v84, v85
	v_cvt_pk_bf16_f32 v123, v80, v81
	v_cvt_pk_bf16_f32 v122, v78, v79
	v_cvt_pk_bf16_f32 v149, v26, v27
	v_cvt_pk_bf16_f32 v148, v22, v23
	v_cvt_pk_bf16_f32 v147, v20, v21
	v_cvt_pk_bf16_f32 v146, v18, v19
	s_waitcnt lgkmcnt(2)
	v_mfma_f32_32x32x16_bf16 v[86:101], v[6:9], v[122:125], v[86:101]
	v_mul_f32_e32 v102, v10, v28
	v_mul_f32_e32 v103, v11, v28
	v_mul_f32_e32 v110, v12, v28
	v_mul_f32_e32 v111, v13, v28
	v_mul_f32_e32 v114, v14, v28
	v_mul_f32_e32 v115, v15, v28
	v_pk_mul_f32 v[156:157], v[16:17], v[28:29] op_sel_hi:[1,0]
	ds_read_b128 v[176:179], v174 offset:33536
	ds_read_b128 v[180:183], v174 offset:33568
	ds_read_b128 v[184:187], v174 offset:33600
	ds_read_b128 v[28:31], v174 offset:33632
	ds_read_b128 v[188:191], v174 offset:33792
	ds_read_b128 v[192:195], v174 offset:33824
	ds_read_b128 v[196:199], v174 offset:33856
	ds_read_b128 v[200:203], v174 offset:33888
	ds_read_b128 v[204:207], v150 offset:62464
	v_cvt_pk_bf16_f32 v133, v56, v57
	v_mfma_f32_32x32x16_bf16 v[34:49], v[6:9], v[146:149], v[34:49]
	v_cvt_pk_bf16_f32 v132, v54, v55
	v_cvt_pk_bf16_f32 v131, v52, v53
	v_cvt_pk_bf16_f32 v130, v50, v51
	ds_read_b128 v[70:73], v174 offset:33664
	ds_read_b128 v[74:77], v174 offset:33920
	ds_read_b128 v[208:211], v150 offset:63488
	v_cvt_pk_bf16_f32 v145, v154, v155
	v_cvt_pk_bf16_f32 v144, v116, v117
	v_cvt_pk_bf16_f32 v143, v112, v113
	v_cvt_pk_bf16_f32 v142, v104, v105
	s_waitcnt lgkmcnt(3)
	v_mfma_f32_32x32x16_bf16 v[86:101], v[204:207], v[130:133], v[86:101]
	v_cvt_pk_bf16_f32 v121, v64, v65
	v_cvt_pk_bf16_f32 v120, v62, v63
	v_cvt_pk_bf16_f32 v119, v60, v61
	v_cvt_pk_bf16_f32 v118, v58, v59
	v_cvt_pk_bf16_f32 v141, v156, v157
	v_cvt_pk_bf16_f32 v140, v114, v115
	v_cvt_pk_bf16_f32 v139, v110, v111
	v_mfma_f32_32x32x16_bf16 v[34:49], v[204:207], v[142:145], v[34:49]
	v_cvt_pk_bf16_f32 v138, v102, v103
	v_fma_f32 v16, v30, v170, v202
	v_fma_f32 v17, v31, v171, v203
	v_fma_f32 v14, v28, v84, v200
	v_fma_f32 v15, v29, v85, v201
	v_pk_fma_f32 v[12:13], v[186:187], v[80:81], v[198:199]
	v_pk_fma_f32 v[10:11], v[184:185], v[78:79], v[196:197]
	v_pk_fma_f32 v[8:9], v[182:183], v[168:169], v[194:195]
	s_waitcnt lgkmcnt(0)
	v_mfma_f32_32x32x16_bf16 v[86:101], v[208:211], v[118:121], v[86:101]
	v_fma_f32 v6, v180, v82, v192
	v_fma_f32 v7, v181, v83, v193
	ds_read_b128 v[78:81], v174 offset:33760
	ds_read_b128 v[82:85], v174 offset:33248
	v_fma_f32 v4, v178, v160, v190
	v_fma_f32 v5, v179, v161, v191
	v_pk_fma_f32 v[2:3], v[176:177], v[158:159], v[188:189]
	v_pk_fma_f32 v[32:33], v[30:31], v[26:27], v[202:203]
	v_pk_fma_f32 v[30:31], v[28:29], v[22:23], v[200:201]
	v_pk_fma_f32 v[28:29], v[186:187], v[20:21], v[198:199]
	v_pk_fma_f32 v[26:27], v[184:185], v[18:19], v[196:197]
	v_pk_fma_f32 v[24:25], v[182:183], v[24:25], v[194:195]
	v_pk_fma_f32 v[22:23], v[180:181], v[166:167], v[192:193]
	v_pk_fma_f32 v[20:21], v[178:179], v[164:165], v[190:191]
	v_pk_fma_f32 v[18:19], v[176:177], v[162:163], v[188:189]
	ds_read_b128 v[158:161], v174 offset:33696
	ds_read_b128 v[162:165], v174 offset:33728
	ds_read_b128 v[166:169], v174 offset:33952
	ds_read_b128 v[176:179], v174 offset:33984
	ds_read_b128 v[180:183], v174 offset:34016
	ds_read_b128 v[184:187], v212 offset:11264
	v_mfma_f32_32x32x16_bf16 v[34:49], v[208:211], v[138:141], v[34:49]
	v_cvt_pk_bf16_f32 v86, v86, v87
	v_cvt_pk_bf16_f32 v87, v88, v89
	v_cvt_pk_bf16_f32 v88, v90, v91
	v_cvt_pk_bf16_f32 v89, v92, v93
	ds_read_b128 v[90:93], v212 offset:12288
	v_pk_max_i16 v86, v86, 0
	v_pk_max_i16 v87, v87, 0
	v_pk_max_i16 v88, v88, 0
	v_pk_max_i16 v89, v89, 0
	s_nop 1
	s_nop 0
	v_cvt_pk_bf16_f32 v188, v34, v35
	v_cvt_pk_bf16_f32 v189, v36, v37
	v_cvt_pk_bf16_f32 v190, v38, v39
	v_cvt_pk_bf16_f32 v191, v40, v41
	s_waitcnt lgkmcnt(1)
	v_mfma_f32_32x32x16_bf16 v[2:17], v[184:187], v[86:89], v[2:17]
	v_pk_max_i16 v188, v188, 0
	v_pk_max_i16 v189, v189, 0
	v_pk_max_i16 v190, v190, 0
	v_pk_max_i16 v191, v191, 0
	v_cvt_pk_bf16_f32 v94, v94, v95
	v_cvt_pk_bf16_f32 v95, v96, v97
	v_cvt_pk_bf16_f32 v96, v98, v99
	v_cvt_pk_bf16_f32 v97, v100, v101
	v_cvt_pk_bf16_f32 v98, v42, v43
	v_cvt_pk_bf16_f32 v99, v44, v45
	v_mfma_f32_32x32x16_bf16 v[18:33], v[184:187], v[188:191], v[18:33]
	ds_read_b128 v[184:187], v212 offset:19456
	v_cvt_pk_bf16_f32 v100, v46, v47
	v_cvt_pk_bf16_f32 v101, v48, v49
	v_fma_f32 v64, v80, v64, v182
	v_fma_f32 v65, v81, v65, v183
	v_pk_fma_f32 v[62:63], v[78:79], v[62:63], v[180:181]
	v_pk_fma_f32 v[60:61], v[164:165], v[60:61], v[178:179]
	v_pk_fma_f32 v[58:59], v[162:163], v[58:59], v[176:177]
	v_pk_max_i16 v94, v94, 0
	v_pk_max_i16 v95, v95, 0
	v_pk_max_i16 v96, v96, 0
	v_pk_max_i16 v97, v97, 0
	v_pk_max_i16 v98, v98, 0
	v_pk_max_i16 v99, v99, 0
	v_pk_max_i16 v100, v100, 0
	v_pk_max_i16 v101, v101, 0
	v_pk_fma_f32 v[56:57], v[160:161], v[56:57], v[168:169]
	s_waitcnt lgkmcnt(1)
	v_mfma_f32_32x32x16_bf16 v[2:17], v[90:93], v[94:97], v[2:17]
	v_fma_f32 v54, v158, v54, v166
	v_fma_f32 v55, v159, v55, v167
	v_fma_f32 v52, v72, v52, v76
	v_fma_f32 v53, v73, v53, v77
	v_fma_f32 v50, v70, v50, v74
	v_fma_f32 v51, v71, v51, v75
	v_pk_fma_f32 v[48:49], v[80:81], v[156:157], v[182:183]
	v_pk_fma_f32 v[46:47], v[78:79], v[114:115], v[180:181]
	v_pk_fma_f32 v[44:45], v[164:165], v[110:111], v[178:179]
	v_pk_fma_f32 v[42:43], v[162:163], v[102:103], v[176:177]
	v_mfma_f32_32x32x16_bf16 v[18:33], v[90:93], v[98:101], v[18:33]
	ds_read_b128 v[90:93], v212 offset:20480
	v_fma_f32 v40, v160, v154, v168
	v_fma_f32 v41, v161, v155, v169
	v_fma_f32 v38, v158, v116, v166
	v_fma_f32 v39, v159, v117, v167
	v_pk_fma_f32 v[36:37], v[72:73], v[112:113], v[76:77]
	v_pk_fma_f32 v[34:35], v[70:71], v[104:105], v[74:75]
	s_waitcnt lgkmcnt(1)
	v_mfma_f32_32x32x16_bf16 v[50:65], v[184:187], v[86:89], v[50:65]
	ds_read_b128 v[70:73], v174 offset:32928
	ds_read_b128 v[74:77], v174 offset:32960
	ds_read_b128 v[78:81], v174 offset:32992
	ds_read_b128 v[86:89], v174 offset:33024
	ds_read_b128 v[110:113], v212 offset:1024
	v_mfma_f32_32x32x16_bf16 v[34:49], v[184:187], v[188:191], v[34:49]
	s_waitcnt lgkmcnt(5)
	v_mfma_f32_32x32x16_bf16 v[50:65], v[90:93], v[94:97], v[50:65]
	v_mfma_f32_32x32x16_bf16 v[34:49], v[90:93], v[98:101], v[34:49]
	s_waitcnt lgkmcnt(2)
	v_mfma_f32_32x32x16_bf16 v[90:105], v[106:109], v[126:129], v[66:81]
	v_mfma_f32_32x32x16_bf16 v[66:81], v[106:109], v[134:137], v[66:81]
	ds_read_b128 v[106:109], v212 offset:0
	s_waitcnt lgkmcnt(0)
	v_mfma_f32_32x32x16_bf16 v[90:105], v[106:109], v[122:125], v[90:105]
	v_mfma_f32_32x32x16_bf16 v[66:81], v[106:109], v[146:149], v[66:81]
	ds_read_b128 v[106:109], v212 offset:2048
	v_mfma_f32_32x32x16_bf16 v[90:105], v[110:113], v[130:133], v[90:105]
	v_mfma_f32_32x32x16_bf16 v[66:81], v[110:113], v[142:145], v[66:81]
	ds_read_b128 v[110:113], v212 offset:13312
	s_waitcnt lgkmcnt(1)
	v_mfma_f32_32x32x16_bf16 v[90:105], v[106:109], v[118:121], v[90:105]
	v_mfma_f32_32x32x16_bf16 v[66:81], v[106:109], v[138:141], v[66:81]
	s_nop 10
	v_cvt_pk_bf16_f32 v90, v90, v91
	v_cvt_pk_bf16_f32 v91, v92, v93
	v_cvt_pk_bf16_f32 v92, v94, v95
	v_cvt_pk_bf16_f32 v94, v98, v99
	v_cvt_pk_bf16_f32 v95, v100, v101
	ds_read_b128 v[98:101], v212 offset:21504
	v_cvt_pk_bf16_f32 v66, v66, v67
	v_cvt_pk_bf16_f32 v67, v68, v69
	v_cvt_pk_bf16_f32 v68, v70, v71
	v_cvt_pk_bf16_f32 v93, v96, v97
	v_cvt_pk_bf16_f32 v69, v72, v73
	ds_read_b128 v[70:73], v212 offset:14336
	v_pk_max_i16 v90, v90, 0
	v_pk_max_i16 v91, v91, 0
	v_pk_max_i16 v92, v92, 0
	v_pk_max_i16 v93, v93, 0
	v_pk_max_i16 v66, v66, 0
	v_pk_max_i16 v67, v67, 0
	v_pk_max_i16 v68, v68, 0
	v_pk_max_i16 v69, v69, 0
	v_cvt_pk_bf16_f32 v96, v102, v103
	s_waitcnt lgkmcnt(2)
	v_mfma_f32_32x32x16_bf16 v[2:17], v[110:113], v[90:93], v[2:17]
	v_cvt_pk_bf16_f32 v97, v104, v105
	v_cvt_pk_bf16_f32 v74, v74, v75
	v_cvt_pk_bf16_f32 v75, v76, v77
	v_cvt_pk_bf16_f32 v76, v78, v79
	v_cvt_pk_bf16_f32 v77, v80, v81
	v_pk_max_i16 v94, v94, 0
	v_pk_max_i16 v95, v95, 0
	v_pk_max_i16 v96, v96, 0
	v_pk_max_i16 v97, v97, 0
	v_pk_max_i16 v74, v74, 0
	v_pk_max_i16 v75, v75, 0
	v_pk_max_i16 v76, v76, 0
	v_pk_max_i16 v77, v77, 0
	v_mfma_f32_32x32x16_bf16 v[18:33], v[110:113], v[66:69], v[18:33]
	s_waitcnt lgkmcnt(1)
	v_mfma_f32_32x32x16_bf16 v[34:49], v[98:101], v[66:69], v[34:49]
	ds_read_b128 v[66:69], v212 offset:22528
	v_mfma_f32_32x32x16_bf16 v[50:65], v[98:101], v[90:93], v[50:65]
	s_waitcnt lgkmcnt(1)
	v_mfma_f32_32x32x16_bf16 v[2:17], v[70:73], v[94:97], v[2:17]
	v_mfma_f32_32x32x16_bf16 v[18:33], v[70:73], v[74:77], v[18:33]
	ds_read_b128 v[78:81], v212 offset:3072
	s_waitcnt lgkmcnt(1)
	v_mfma_f32_32x32x16_bf16 v[50:65], v[66:69], v[94:97], v[50:65]
	ds_read_b128 v[90:93], v174 offset:33056
	ds_read_b128 v[94:97], v174 offset:33088
	ds_read_b128 v[98:101], v174 offset:33120
	ds_read_b128 v[70:73], v174 offset:33152
	v_mfma_f32_32x32x16_bf16 v[34:49], v[66:69], v[74:77], v[34:49]
	ds_read_b128 v[66:69], v212 offset:4096
	ds_read_b128 v[74:77], v212 offset:5120
	s_waitcnt lgkmcnt(3)
	v_mfma_f32_32x32x16_bf16 v[102:117], v[78:81], v[126:129], v[86:101]
	v_mfma_f32_32x32x16_bf16 v[86:101], v[78:81], v[134:137], v[86:101]
	s_waitcnt lgkmcnt(1)
	v_mfma_f32_32x32x16_bf16 v[86:101], v[66:69], v[146:149], v[86:101]
	v_mfma_f32_32x32x16_bf16 v[102:117], v[66:69], v[122:125], v[102:117]
	ds_read_b128 v[66:69], v212 offset:6144
	s_waitcnt lgkmcnt(1)
	v_mfma_f32_32x32x16_bf16 v[86:101], v[74:77], v[142:145], v[86:101]
	v_mfma_f32_32x32x16_bf16 v[102:117], v[74:77], v[130:133], v[102:117]
	ds_read_b128 v[74:77], v212 offset:15360
	s_waitcnt lgkmcnt(1)
	v_mfma_f32_32x32x16_bf16 v[86:101], v[66:69], v[138:141], v[86:101]
	v_mfma_f32_32x32x16_bf16 v[102:117], v[66:69], v[118:121], v[102:117]
	s_nop 10
	v_cvt_pk_bf16_f32 v78, v86, v87
	v_cvt_pk_bf16_f32 v80, v90, v91
	v_cvt_pk_bf16_f32 v79, v88, v89
	v_cvt_pk_bf16_f32 v81, v92, v93
	ds_read_b128 v[86:89], v212 offset:16384
	ds_read_b128 v[90:93], v212 offset:23552
	v_cvt_pk_bf16_f32 v66, v102, v103
	v_cvt_pk_bf16_f32 v67, v104, v105
	v_cvt_pk_bf16_f32 v68, v106, v107
	v_cvt_pk_bf16_f32 v69, v108, v109
	v_pk_max_i16 v66, v66, 0
	v_pk_max_i16 v67, v67, 0
	v_pk_max_i16 v68, v68, 0
	v_pk_max_i16 v69, v69, 0
	v_pk_max_i16 v78, v78, 0
	v_pk_max_i16 v79, v79, 0
	v_pk_max_i16 v80, v80, 0
	v_pk_max_i16 v81, v81, 0
	v_cvt_pk_bf16_f32 v94, v94, v95
	s_waitcnt lgkmcnt(2)
	v_mfma_f32_32x32x16_bf16 v[18:33], v[74:77], v[78:81], v[18:33]
	v_cvt_pk_bf16_f32 v95, v96, v97
	v_cvt_pk_bf16_f32 v96, v98, v99
	v_cvt_pk_bf16_f32 v97, v100, v101
	v_pk_max_i16 v94, v94, 0
	v_pk_max_i16 v95, v95, 0
	v_pk_max_i16 v96, v96, 0
	v_pk_max_i16 v97, v97, 0
	v_mfma_f32_32x32x16_bf16 v[2:17], v[74:77], v[66:69], v[2:17]
	v_cvt_pk_bf16_f32 v74, v110, v111
	v_cvt_pk_bf16_f32 v75, v112, v113
	v_cvt_pk_bf16_f32 v76, v114, v115
	v_cvt_pk_bf16_f32 v77, v116, v117
	v_pk_max_i16 v74, v74, 0
	v_pk_max_i16 v75, v75, 0
	v_pk_max_i16 v76, v76, 0
	v_pk_max_i16 v77, v77, 0
	s_waitcnt lgkmcnt(0)
	v_mfma_f32_32x32x16_bf16 v[50:65], v[90:93], v[66:69], v[50:65]
	ds_read_b128 v[66:69], v212 offset:24576
	v_mfma_f32_32x32x16_bf16 v[34:49], v[90:93], v[78:81], v[34:49]
	ds_read_b128 v[102:105], v212 offset:7168
	v_mfma_f32_32x32x16_bf16 v[2:17], v[86:89], v[74:77], v[2:17]
	s_waitcnt lgkmcnt(1)
	v_mfma_f32_32x32x16_bf16 v[50:65], v[66:69], v[74:77], v[50:65]
	ds_read_b128 v[74:77], v174 offset:33184
	ds_read_b128 v[78:81], v174 offset:33216
	v_mfma_f32_32x32x16_bf16 v[34:49], v[66:69], v[94:97], v[34:49]
	ds_read_b128 v[66:69], v212 offset:8192
	v_mfma_f32_32x32x16_bf16 v[18:33], v[86:89], v[94:97], v[18:33]
	s_waitcnt lgkmcnt(1)
	v_mfma_f32_32x32x16_bf16 v[86:101], v[102:105], v[126:129], v[70:85]
	v_mfma_f32_32x32x16_bf16 v[70:85], v[102:105], v[134:137], v[70:85]
	ds_read_b128 v[102:105], v212 offset:9216
	v_lshlrev_b32_e32 v135, 2, v1
	v_add_u32_e32 v134, v172, v174
	s_waitcnt lgkmcnt(1)
	v_mfma_f32_32x32x16_bf16 v[86:101], v[66:69], v[122:125], v[86:101]
	v_mfma_f32_32x32x16_bf16 v[70:85], v[66:69], v[146:149], v[70:85]
	ds_read_b128 v[66:69], v212 offset:10240
	s_waitcnt lgkmcnt(1)
	v_mfma_f32_32x32x16_bf16 v[86:101], v[102:105], v[130:133], v[86:101]
	v_mfma_f32_32x32x16_bf16 v[70:85], v[102:105], v[142:145], v[70:85]
	ds_read_b128 v[102:105], v212 offset:17408
	s_waitcnt lgkmcnt(1)
	v_mfma_f32_32x32x16_bf16 v[86:101], v[66:69], v[118:121], v[86:101]
	v_mfma_f32_32x32x16_bf16 v[70:85], v[66:69], v[138:141], v[70:85]
	s_nop 10
	v_cvt_pk_bf16_f32 v68, v90, v91
	v_cvt_pk_bf16_f32 v69, v92, v93
	ds_read_b128 v[90:93], v212 offset:25600
	v_cvt_pk_bf16_f32 v66, v86, v87
	v_cvt_pk_bf16_f32 v67, v88, v89
	v_pk_max_i16 v66, v66, 0
	v_pk_max_i16 v67, v67, 0
	v_pk_max_i16 v68, v68, 0
	v_pk_max_i16 v69, v69, 0
	v_cvt_pk_bf16_f32 v70, v70, v71
	v_cvt_pk_bf16_f32 v71, v72, v73
	s_waitcnt lgkmcnt(1)
	v_mfma_f32_32x32x16_bf16 v[2:17], v[102:105], v[66:69], v[2:17]
	v_cvt_pk_bf16_f32 v72, v74, v75
	v_cvt_pk_bf16_f32 v73, v76, v77
	ds_read_b128 v[74:77], v212 offset:18432
	v_cvt_pk_bf16_f32 v86, v94, v95
	v_cvt_pk_bf16_f32 v87, v96, v97
	v_cvt_pk_bf16_f32 v88, v98, v99
	s_waitcnt lgkmcnt(1)
	v_mfma_f32_32x32x16_bf16 v[50:65], v[90:93], v[66:69], v[50:65]
	ds_read_b128 v[66:69], v212 offset:26624
	v_cvt_pk_bf16_f32 v89, v100, v101
	v_pk_max_i16 v86, v86, 0
	v_pk_max_i16 v87, v87, 0
	v_pk_max_i16 v88, v88, 0
	v_pk_max_i16 v89, v89, 0
	v_pk_max_i16 v70, v70, 0
	v_pk_max_i16 v71, v71, 0
	v_pk_max_i16 v72, v72, 0
	v_pk_max_i16 v73, v73, 0
	v_cvt_pk_bf16_f32 v78, v78, v79
	v_cvt_pk_bf16_f32 v79, v80, v81
	s_waitcnt lgkmcnt(1)
	v_mfma_f32_32x32x16_bf16 v[2:17], v[74:77], v[86:89], v[2:17]
	v_cvt_pk_bf16_f32 v80, v82, v83
	v_cvt_pk_bf16_f32 v81, v84, v85
	v_pk_max_i16 v78, v78, 0
	v_pk_max_i16 v79, v79, 0
	v_pk_max_i16 v80, v80, 0
	v_pk_max_i16 v81, v81, 0
	s_waitcnt lgkmcnt(0)
	v_mfma_f32_32x32x16_bf16 v[50:65], v[66:69], v[86:89], v[50:65]
	v_mfma_f32_32x32x16_bf16 v[34:49], v[90:93], v[70:73], v[34:49]
	s_nop 10
	v_add_f32_e32 v130, v10, v58
	v_add_f32_e32 v131, v11, v59
	v_add_f32_e32 v132, v12, v60
	v_add_f32_e32 v133, v13, v61
	v_add_f32_e32 v138, v4, v52
	v_add_f32_e32 v139, v5, v53
	v_pk_add_f32 v[140:141], v[16:17], v[64:65]
	v_pk_add_f32 v[142:143], v[8:9], v[56:57]
	v_pk_add_f32 v[144:145], v[14:15], v[62:63]
	v_pk_add_f32 v[146:147], v[6:7], v[54:55]
	v_mfma_f32_32x32x16_bf16 v[18:33], v[102:105], v[70:73], v[18:33]
	ds_read2st64_b32 v[70:71], v135 offset0:133 offset1:134
	v_add_f32_e32 v148, v2, v50
	v_add_f32_e32 v149, v3, v51
	v_add_f32_e32 v144, v146, v144
	v_add_f32_e32 v145, v147, v145
	v_pk_add_f32 v[140:141], v[142:143], v[140:141]
	v_pk_add_f32 v[132:133], v[138:139], v[132:133]
	v_pk_add_f32 v[130:131], v[148:149], v[130:131]
	v_pk_add_f32 v[132:133], v[132:133], v[140:141]
	v_pk_add_f32 v[130:131], v[130:131], v[144:145]
	v_mfma_f32_32x32x16_bf16 v[34:49], v[66:69], v[78:81], v[34:49]
	v_pk_mov_b32 v[138:139], v[130:131], v[132:133] op_sel:[1,0]
	v_mov_b32_e32 v131, v133
	s_waitcnt vmcnt(0) lgkmcnt(0)
	v_mul_f32_e32 v66, v175, v70
	v_pk_add_f32 v[130:131], v[138:139], v[130:131]
	ds_write_b32 v173, v66 offset:512
	v_mul_f32_e32 v66, v175, v71
	v_pk_add_f32 v[130:131], v[130:131], v[130:131] op_sel:[0,1] op_sel_hi:[1,0]
	s_waitcnt lgkmcnt(0)
	ds_read_b128 v[102:105], v174 offset:34560
	ds_read_b128 v[98:101], v174 offset:34592
	ds_read_b128 v[110:113], v174 offset:34624
	ds_read_b128 v[106:109], v174 offset:34656
	ds_read_b128 v[114:117], v174 offset:34688
	ds_read_b128 v[122:125], v174 offset:34720
	ds_read_b128 v[118:121], v174 offset:34752
	ds_read_b128 v[126:129], v174 offset:34784
	v_mov_b32_dpp v66, v66 quad_perm:[1,0,3,2] row_mask:0xf bank_mask:0xf bound_ctrl:1
	v_mov_b32_e32 v131, v130
	v_fmac_f32_e32 v66, v175, v71
	s_nop 0
	v_permlane32_swap_b32_e32 v130, v131
	v_add_f32_dpp v66, v66, v66 quad_perm:[2,3,0,1] row_mask:0xf bank_mask:0xf bound_ctrl:1
	v_add_f32_e32 v130, v130, v131
	v_fmamk_f32 v65, v130, 0xbc800000, v65
	v_add_f32_dpp v66, v66, v66 row_half_mirror row_mask:0xf bank_mask:0xf bound_ctrl:1
	v_fmamk_f32 v64, v130, 0xbc800000, v64
	v_fmamk_f32 v63, v130, 0xbc800000, v63
	v_fmamk_f32 v62, v130, 0xbc800000, v62
	v_fmamk_f32 v61, v130, 0xbc800000, v61
	v_fmamk_f32 v60, v130, 0xbc800000, v60
	v_fmamk_f32 v59, v130, 0xbc800000, v59
	v_fmamk_f32 v58, v130, 0xbc800000, v58
	v_fmamk_f32 v57, v130, 0xbc800000, v57
	v_fmamk_f32 v56, v130, 0xbc800000, v56
	v_fmamk_f32 v55, v130, 0xbc800000, v55
	v_fmamk_f32 v54, v130, 0xbc800000, v54
	v_fmamk_f32 v53, v130, 0xbc800000, v53
	v_fmamk_f32 v52, v130, 0xbc800000, v52
	v_fmamk_f32 v51, v130, 0xbc800000, v51
	v_fmac_f32_e32 v50, 0xbc800000, v130
	v_add_f32_dpp v66, v66, v66 row_ror:8 row_mask:0xf bank_mask:0xf bound_ctrl:1
	v_fmamk_f32 v17, v130, 0xbc800000, v17
	v_fmamk_f32 v16, v130, 0xbc800000, v16
	v_fmamk_f32 v15, v130, 0xbc800000, v15
	v_fmamk_f32 v14, v130, 0xbc800000, v14
	v_fmamk_f32 v13, v130, 0xbc800000, v13
	v_fmamk_f32 v12, v130, 0xbc800000, v12
	v_fmamk_f32 v11, v130, 0xbc800000, v11
	v_fmamk_f32 v10, v130, 0xbc800000, v10
	v_fmamk_f32 v9, v130, 0xbc800000, v9
	v_fmamk_f32 v8, v130, 0xbc800000, v8
	v_fmamk_f32 v7, v130, 0xbc800000, v7
	v_fmamk_f32 v6, v130, 0xbc800000, v6
	v_fmamk_f32 v5, v130, 0xbc800000, v5
	v_fmamk_f32 v4, v130, 0xbc800000, v4
	v_fmamk_f32 v3, v130, 0xbc800000, v3
	v_fmac_f32_e32 v2, 0xbc800000, v130
	v_pk_mul_f32 v[130:131], v[54:55], v[54:55]
	v_pk_mul_f32 v[132:133], v[62:63], v[62:63]
	v_pk_mul_f32 v[138:139], v[50:51], v[50:51]
	v_pk_mul_f32 v[140:141], v[58:59], v[58:59]
	v_pk_mul_f32 v[142:143], v[56:57], v[56:57]
	v_pk_mul_f32 v[144:145], v[64:65], v[64:65]
	v_pk_mul_f32 v[146:147], v[52:53], v[52:53]
	v_pk_mul_f32 v[148:149], v[60:61], v[60:61]
	v_mov_b32_e32 v67, v66
	v_pk_fma_f32 v[148:149], v[12:13], v[12:13], v[148:149]
	v_pk_fma_f32 v[146:147], v[4:5], v[4:5], v[146:147]
	v_pk_fma_f32 v[144:145], v[16:17], v[16:17], v[144:145]
	v_pk_fma_f32 v[142:143], v[8:9], v[8:9], v[142:143]
	v_pk_fma_f32 v[140:141], v[10:11], v[10:11], v[140:141]
	v_pk_fma_f32 v[138:139], v[2:3], v[2:3], v[138:139]
	v_pk_fma_f32 v[132:133], v[14:15], v[14:15], v[132:133]
	v_pk_fma_f32 v[130:131], v[6:7], v[6:7], v[130:131]
	v_permlane16_swap_b32_e32 v66, v67
	v_pk_add_f32 v[130:131], v[130:131], v[132:133]
	v_pk_add_f32 v[132:133], v[138:139], v[140:141]
	v_pk_add_f32 v[138:139], v[142:143], v[144:145]
	v_pk_add_f32 v[140:141], v[146:147], v[148:149]
	v_mfma_f32_32x32x16_bf16 v[18:33], v[74:77], v[78:81], v[18:33]
	v_add_f32_e32 v136, v66, v67
	ds_read_b128 v[70:73], v134 offset:512
	ds_read_b128 v[66:69], v134 offset:544
	ds_read_b128 v[78:81], v134 offset:576
	ds_read_b128 v[74:77], v134 offset:608
	ds_read_b128 v[82:85], v134 offset:640
	ds_read_b128 v[90:93], v134 offset:672
	ds_read_b128 v[86:89], v134 offset:704
	ds_read_b128 v[94:97], v134 offset:736
	v_pk_add_f32 v[138:139], v[140:141], v[138:139]
	v_pk_add_f32 v[130:131], v[132:133], v[130:131]
	s_waitcnt lgkmcnt(8)
	v_pk_mul_f32 v[140:141], v[126:127], v[62:63]
	v_pk_mov_b32 v[132:133], v[130:131], v[138:139] op_sel:[1,0]
	v_mov_b32_e32 v131, v139
	v_pk_mul_f32 v[138:139], v[122:123], v[54:55]
	v_pk_mul_f32 v[142:143], v[114:115], v[50:51]
	v_pk_mul_f32 v[144:145], v[118:119], v[58:59]
	v_pk_mul_f32 v[146:147], v[124:125], v[56:57]
	v_pk_mul_f32 v[148:149], v[128:129], v[64:65]
	v_pk_mul_f32 v[154:155], v[116:117], v[52:53]
	v_pk_mul_f32 v[156:157], v[120:121], v[60:61]
	v_pk_fma_f32 v[154:155], v[104:105], v[4:5], v[154:155]
	v_pk_fma_f32 v[156:157], v[112:113], v[12:13], v[156:157]
	v_pk_fma_f32 v[148:149], v[108:109], v[16:17], v[148:149]
	v_pk_fma_f32 v[146:147], v[100:101], v[8:9], v[146:147]
	v_pk_fma_f32 v[144:145], v[110:111], v[10:11], v[144:145]
	v_pk_fma_f32 v[142:143], v[102:103], v[2:3], v[142:143]
	v_pk_fma_f32 v[140:141], v[106:107], v[14:15], v[140:141]
	v_pk_fma_f32 v[138:139], v[98:99], v[6:7], v[138:139]
	v_pk_add_f32 v[130:131], v[132:133], v[130:131]
	v_pk_add_f32 v[138:139], v[138:139], v[140:141]
	v_pk_add_f32 v[140:141], v[142:143], v[144:145]
	v_pk_add_f32 v[142:143], v[146:147], v[148:149]
	v_pk_add_f32 v[144:145], v[154:155], v[156:157]
	v_pk_add_f32 v[132:133], v[130:131], v[130:131] op_sel:[0,1] op_sel_hi:[1,0]
	v_pk_add_f32 v[142:143], v[144:145], v[142:143]
	v_pk_add_f32 v[138:139], v[140:141], v[138:139]
	v_add_f32_e32 v133, v142, v143
	v_add_f32_e32 v130, v138, v139
	s_waitcnt lgkmcnt(2)
	v_pk_mul_f32 v[138:139], v[90:91], v[54:55]
	s_waitcnt lgkmcnt(0)
	v_pk_mul_f32 v[140:141], v[94:95], v[62:63]
	v_pk_mul_f32 v[142:143], v[82:83], v[50:51]
	v_pk_mul_f32 v[144:145], v[86:87], v[58:59]
	v_pk_mul_f32 v[146:147], v[92:93], v[56:57]
	v_pk_mul_f32 v[148:149], v[96:97], v[64:65]
	v_pk_mul_f32 v[154:155], v[84:85], v[52:53]
	v_pk_mul_f32 v[156:157], v[88:89], v[60:61]
	v_add_f32_e32 v130, v130, v133
	v_pk_fma_f32 v[156:157], v[80:81], v[12:13], v[156:157]
	v_pk_fma_f32 v[154:155], v[72:73], v[4:5], v[154:155]
	v_pk_fma_f32 v[148:149], v[76:77], v[16:17], v[148:149]
	v_pk_fma_f32 v[146:147], v[68:69], v[8:9], v[146:147]
	v_pk_fma_f32 v[144:145], v[78:79], v[10:11], v[144:145]
	v_pk_fma_f32 v[142:143], v[70:71], v[2:3], v[142:143]
	v_pk_fma_f32 v[140:141], v[74:75], v[14:15], v[140:141]
	v_pk_fma_f32 v[138:139], v[66:67], v[6:7], v[138:139]
	v_mov_b32_e32 v133, v130
	v_pk_add_f32 v[138:139], v[138:139], v[140:141]
	v_pk_add_f32 v[140:141], v[142:143], v[144:145]
	v_pk_add_f32 v[142:143], v[146:147], v[148:149]
	v_pk_add_f32 v[144:145], v[154:155], v[156:157]
	v_permlane32_swap_b32_e32 v130, v133
	v_pk_add_f32 v[142:143], v[144:145], v[142:143]
	v_add_f32_e32 v160, v130, v133
	v_pk_add_f32 v[138:139], v[140:141], v[138:139]
	v_add_f32_e32 v133, v142, v143
	v_pk_add_f32 v[140:141], v[26:27], v[42:43]
	v_pk_add_f32 v[142:143], v[28:29], v[44:45]
	v_pk_add_f32 v[144:145], v[20:21], v[36:37]
	v_pk_add_f32 v[146:147], v[32:33], v[48:49]
	v_pk_add_f32 v[148:149], v[24:25], v[40:41]
	v_pk_add_f32 v[154:155], v[30:31], v[46:47]
	v_pk_add_f32 v[156:157], v[22:23], v[38:39]
	v_pk_add_f32 v[158:159], v[18:19], v[34:35]
	v_pk_add_f32 v[154:155], v[156:157], v[154:155]
	v_pk_add_f32 v[146:147], v[148:149], v[146:147]
	v_pk_add_f32 v[142:143], v[144:145], v[142:143]
	v_pk_add_f32 v[140:141], v[158:159], v[140:141]
	v_pk_add_f32 v[142:143], v[142:143], v[146:147]
	v_pk_add_f32 v[140:141], v[140:141], v[154:155]
	v_add_f32_e32 v130, v138, v139
	v_pk_mov_b32 v[144:145], v[140:141], v[142:143] op_sel:[1,0]
	v_mov_b32_e32 v141, v143
	v_pk_add_f32 v[140:141], v[144:145], v[140:141]
	v_add_f32_e32 v133, v130, v133
	v_pk_add_f32 v[140:141], v[140:141], v[140:141] op_sel:[0,1] op_sel_hi:[1,0]
	v_mov_b32_e32 v131, v132
	v_mov_b32_e32 v130, v140
	s_nop 1
	v_permlane32_swap_b32_e32 v140, v130
	v_add_f32_e32 v130, v140, v130
	v_fmamk_f32 v49, v130, 0xbc800000, v49
	v_fmamk_f32 v48, v130, 0xbc800000, v48
	v_fmamk_f32 v47, v130, 0xbc800000, v47
	v_fmamk_f32 v46, v130, 0xbc800000, v46
	v_fmamk_f32 v45, v130, 0xbc800000, v45
	v_fmamk_f32 v44, v130, 0xbc800000, v44
	v_fmamk_f32 v43, v130, 0xbc800000, v43
	v_fmamk_f32 v42, v130, 0xbc800000, v42
	v_fmamk_f32 v41, v130, 0xbc800000, v41
	v_fmamk_f32 v40, v130, 0xbc800000, v40
	v_fmamk_f32 v39, v130, 0xbc800000, v39
	v_fmamk_f32 v38, v130, 0xbc800000, v38
	v_fmamk_f32 v37, v130, 0xbc800000, v37
	v_fmamk_f32 v36, v130, 0xbc800000, v36
	v_fmamk_f32 v35, v130, 0xbc800000, v35
	v_fmac_f32_e32 v34, 0xbc800000, v130
	v_fmamk_f32 v33, v130, 0xbc800000, v33
	v_fmamk_f32 v32, v130, 0xbc800000, v32
	v_fmamk_f32 v31, v130, 0xbc800000, v31
	v_fmamk_f32 v30, v130, 0xbc800000, v30
	v_fmamk_f32 v29, v130, 0xbc800000, v29
	v_fmamk_f32 v28, v130, 0xbc800000, v28
	v_fmamk_f32 v27, v130, 0xbc800000, v27
	v_fmamk_f32 v26, v130, 0xbc800000, v26
	v_fmamk_f32 v25, v130, 0xbc800000, v25
	v_fmamk_f32 v24, v130, 0xbc800000, v24
	v_fmamk_f32 v23, v130, 0xbc800000, v23
	v_fmamk_f32 v22, v130, 0xbc800000, v22
	v_fmamk_f32 v21, v130, 0xbc800000, v21
	v_fmamk_f32 v20, v130, 0xbc800000, v20
	v_fmamk_f32 v19, v130, 0xbc800000, v19
	v_fmac_f32_e32 v18, 0xbc800000, v130
	v_pk_mul_f32 v[140:141], v[38:39], v[38:39]
	v_pk_mul_f32 v[142:143], v[46:47], v[46:47]
	v_pk_mul_f32 v[144:145], v[34:35], v[34:35]
	v_pk_mul_f32 v[146:147], v[42:43], v[42:43]
	v_pk_mul_f32 v[148:149], v[40:41], v[40:41]
	v_pk_mul_f32 v[154:155], v[48:49], v[48:49]
	v_pk_mul_f32 v[156:157], v[36:37], v[36:37]
	v_pk_mul_f32 v[158:159], v[44:45], v[44:45]
	v_pk_fma_f32 v[156:157], v[20:21], v[20:21], v[156:157]
	v_pk_fma_f32 v[158:159], v[28:29], v[28:29], v[158:159]
	v_pk_fma_f32 v[154:155], v[32:33], v[32:33], v[154:155]
	v_pk_fma_f32 v[148:149], v[24:25], v[24:25], v[148:149]
	v_pk_fma_f32 v[146:147], v[26:27], v[26:27], v[146:147]
	v_pk_fma_f32 v[144:145], v[18:19], v[18:19], v[144:145]
	v_pk_fma_f32 v[142:143], v[30:31], v[30:31], v[142:143]
	v_pk_fma_f32 v[140:141], v[22:23], v[22:23], v[140:141]
	v_permlane32_swap_b32_e32 v132, v131
	v_pk_add_f32 v[140:141], v[140:141], v[142:143]
	v_pk_add_f32 v[142:143], v[144:145], v[146:147]
	v_pk_add_f32 v[144:145], v[148:149], v[154:155]
	v_pk_add_f32 v[146:147], v[156:157], v[158:159]
	v_pk_add_f32 v[140:141], v[142:143], v[140:141]
	v_pk_add_f32 v[144:145], v[146:147], v[144:145]
	v_pk_mul_f32 v[122:123], v[122:123], v[38:39]
	v_pk_mov_b32 v[142:143], v[140:141], v[144:145] op_sel:[1,0]
	v_mov_b32_e32 v141, v145
	v_pk_add_f32 v[140:141], v[142:143], v[140:141]
	v_pk_mul_f32 v[126:127], v[126:127], v[46:47]
	v_pk_add_f32 v[140:141], v[140:141], v[140:141] op_sel:[0,1] op_sel_hi:[1,0]
	v_pk_mul_f32 v[114:115], v[114:115], v[34:35]
	v_mov_b32_e32 v130, v140
	s_nop 1
	v_permlane32_swap_b32_e32 v140, v130
	v_mov_b32_e32 v141, v132
	v_pk_add_f32 v[130:131], v[140:141], v[130:131]
	v_pk_mul_f32 v[118:119], v[118:119], v[42:43]
	v_pk_fma_f32 v[130:131], v[130:131], s[0:1], v[152:153] op_sel_hi:[1,0,0]
	v_pk_mul_f32 v[124:125], v[124:125], v[40:41]
	v_mul_f32_e32 v132, 0x4b800000, v131
	v_cmp_gt_f32_e32 vcc, s1, v131
	v_pk_mul_f32 v[128:129], v[128:129], v[48:49]
	v_pk_mul_f32 v[116:117], v[116:117], v[36:37]
	v_pk_mul_f32 v[120:121], v[120:121], v[44:45]
	v_cndmask_b32_e32 v131, v131, v132, vcc
	v_mul_f32_e32 v132, 0x4b800000, v130
	v_cmp_gt_f32_e64 s[0:1], s1, v130
	v_pk_fma_f32 v[112:113], v[112:113], v[28:29], v[120:121]
	v_pk_fma_f32 v[104:105], v[104:105], v[20:21], v[116:117]
	v_pk_fma_f32 v[108:109], v[108:109], v[32:33], v[128:129]
	v_pk_fma_f32 v[100:101], v[100:101], v[24:25], v[124:125]
	v_pk_fma_f32 v[110:111], v[110:111], v[26:27], v[118:119]
	v_pk_fma_f32 v[102:103], v[102:103], v[18:19], v[114:115]
	v_pk_fma_f32 v[106:107], v[106:107], v[30:31], v[126:127]
	v_pk_fma_f32 v[98:99], v[98:99], v[22:23], v[122:123]
	v_rsq_f32_e32 v131, v131
	v_cndmask_b32_e64 v130, v130, v132, s[0:1]
	v_pk_add_f32 v[98:99], v[98:99], v[106:107]
	v_pk_add_f32 v[102:103], v[102:103], v[110:111]
	v_pk_add_f32 v[100:101], v[100:101], v[108:109]
	v_pk_add_f32 v[104:105], v[104:105], v[112:113]
	v_rsq_f32_e32 v132, v130
	v_pk_add_f32 v[100:101], v[104:105], v[100:101]
	v_pk_add_f32 v[98:99], v[102:103], v[98:99]
	v_mul_f32_e32 v130, 0x45800000, v131
	v_add_f32_e32 v98, v98, v99
	v_add_f32_e32 v99, v100, v101
	v_add_f32_e32 v98, v98, v99
	v_mov_b32_e32 v99, v98
	v_pk_mul_f32 v[90:91], v[90:91], v[38:39]
	v_pk_mul_f32 v[94:95], v[94:95], v[46:47]
	v_pk_mul_f32 v[82:83], v[82:83], v[34:35]
	v_pk_mul_f32 v[86:87], v[86:87], v[42:43]
	v_cndmask_b32_e32 v130, v131, v130, vcc
	v_mul_f32_e32 v131, 0x45800000, v132
	v_permlane32_swap_b32_e32 v98, v99
	v_pk_fma_f32 v[78:79], v[78:79], v[26:27], v[86:87]
	v_pk_fma_f32 v[70:71], v[70:71], v[18:19], v[82:83]
	v_pk_fma_f32 v[74:75], v[74:75], v[30:31], v[94:95]
	v_pk_fma_f32 v[66:67], v[66:67], v[22:23], v[90:91]
	v_cndmask_b32_e64 v131, v132, v131, s[0:1]
	v_add_f32_e32 v98, v98, v99
	v_pk_add_f32 v[66:67], v[66:67], v[74:75]
	v_pk_add_f32 v[70:71], v[70:71], v[78:79]
	v_mul_f32_e32 v139, v160, v130
	v_mul_f32_e32 v98, v98, v131
	v_pk_add_f32 v[66:67], v[70:71], v[66:67]
	v_cmp_gt_u32_e32 vcc, 32, v1
	v_add_f32_e32 v66, v66, v67
	v_pk_mul_f32 v[92:93], v[92:93], v[40:41]
	v_cndmask_b32_e32 v67, v98, v139, vcc
	v_add_f32_e32 v67, s12, v67
	v_pk_mul_f32 v[96:97], v[96:97], v[48:49]
	v_pk_mul_f32 v[84:85], v[84:85], v[36:37]
	v_pk_mul_f32 v[88:89], v[88:89], v[44:45]
	v_mul_f32_e32 v67, 0xbfb8aa3b, v67
	v_pk_fma_f32 v[80:81], v[80:81], v[28:29], v[88:89]
	v_pk_fma_f32 v[72:73], v[72:73], v[20:21], v[84:85]
	v_pk_fma_f32 v[76:77], v[76:77], v[32:33], v[96:97]
	v_pk_fma_f32 v[68:69], v[68:69], v[24:25], v[92:93]
	v_exp_f32_e32 v70, v67
	v_pk_add_f32 v[68:69], v[68:69], v[76:77]
	v_pk_add_f32 v[72:73], v[72:73], v[80:81]
	v_cmp_lt_i32_e64 s[0:1], 0, v151
	v_pk_add_f32 v[68:69], v[72:73], v[68:69]
	v_mov_b32_e32 v137, v136
	v_add_f32_e32 v67, v68, v69
	v_add_f32_e32 v67, v66, v67
	v_add_f32_e32 v66, 1.0, v70
	v_rcp_f32_e32 v66, v66
	v_mov_b32_e32 v69, 0xff800000
	v_mov_b32_e32 v138, v133
	v_mov_b32_e32 v68, v67
	v_cndmask_b32_e64 v70, v69, v66, s[0:1]
	v_mbcnt_lo_u32_b32 v66, -1, 0
	v_mbcnt_hi_u32_b32 v66, -1, v66
	v_permlane32_swap_b32_e32 v136, v137
	v_permlane32_swap_b32_e32 v133, v138
	v_permlane32_swap_b32_e32 v67, v68
	v_and_b32_e32 v86, 64, v66
	s_mov_b32 s14, 8
	s_mov_b32 s13, 0
	v_mov_b32_e32 v66, 0
	s_waitcnt lgkmcnt(0)
